# speedup vs baseline: 1.0068x; 1.0068x over previous
_Z11prep_kernelPKfS0_S0_S0_S0_S0_S0_S0_S0_PKiPDv8_DF16bS4_PfS5_S5_PiPt:
	s_load_dwordx4 s[16:19], s[0:1], 0x0
	s_load_dwordx4 s[20:23], s[0:1], 0x10
	s_load_dwordx4 s[24:27], s[0:1], 0x20
	s_load_dwordx4 s[28:31], s[0:1], 0x30
	s_load_dwordx4 s[32:35], s[0:1], 0x40
	s_load_dwordx2 s[36:37], s[0:1], 0x80
	v_and_b32_e32 v126, 63, v0
	v_lshrrev_b32_e32 v128, 6, v0
	v_and_b32_e32 v1, 15, v0
	v_bfe_u32 v24, v0, 4, 2
	v_lshl_or_b32 v107, v128, 4, v1
	v_lshlrev_b32_e32 v106, 2, v107
	v_lshlrev_b32_e32 v127, 2, v0
	v_lshlrev_b32_e32 v25, 1, v107
	v_and_b32_e32 v26, 48, v0
	v_mul_u32_u24_e32 v27, 0x440, v24
	v_lshlrev_b32_e32 v120, 4, v0
	v_lshrrev_b32_e32 v58, 5, v0
	v_mul_u32_u24_e32 v58, 0x110, v58
	v_and_b32_e32 v125, 31, v0
	v_lshl_add_u32 v58, v125, 3, v58
	v_add_u32_e32 v124, 0x1b400, v58
	v_mul_u32_u24_e32 v52, 0x110, v1
	v_add_u32_e32 v52, v52, v26
	v_add_u32_e32 v53, 0x1b400, v52
	v_add_u32_e32 v54, 0x1c500, v52
	v_add_u32_e32 v55, v27, v25
	v_add_u32_e32 v55, 0x1c500, v55
	v_mul_u32_u24_e32 v56, 0x110, v107
	v_add_u32_e32 v56, v56, v26
	v_add_u32_e32 v57, 0x8800, v56
	s_lshl_b32 s12, s2, 4
	s_add_i32 s3, s12, 0xfffff800
	s_cmpk_gt_i32 s2, 0x7f
	s_cselect_b64 s[6:7], -1, 0
	s_mov_b32 s48, 0
	s_mov_b32 s49, -1
	v_lshl_or_b32 v123, s2, 3, v128
	v_lshlrev_b32_e32 v123, 12, v123
	v_lshl_add_u32 v123, v126, 4, v123
	s_waitcnt lgkmcnt(0)
	s_cmpk_lt_i32 s2, 0x80
	s_cselect_b32 s38, s16, s18
	s_cselect_b32 s39, s17, s19
	s_cselect_b32 s40, s20, s24
	s_cselect_b32 s41, s21, s25
	s_cselect_b32 s13, s12, s3
	s_cselect_b32 s44, 0x3db504f3, 1.0
	s_lshl_b32 s13, s13, 9
	s_add_u32 s38, s38, s13
	s_addc_u32 s39, s39, 0
	global_load_dwordx4 v[2:5], v120, s[38:39] nt
	s_and_b32 s13, s2, 7
	s_lshl_b32 s14, s13, 13
	v_add_u32_e32 v125, s14, v120
	global_load_dwordx4 v[80:83], v125, s[40:41]
	s_add_i32 s13, s2, 1
	s_and_b32 s13, s13, 7
	s_lshl_b32 s14, s13, 13
	v_add_u32_e32 v125, s14, v120
	global_load_dwordx4 v[84:87], v125, s[40:41]
	s_add_i32 s13, s2, 2
	s_and_b32 s13, s13, 7
	s_lshl_b32 s14, s13, 13
	v_add_u32_e32 v125, s14, v120
	global_load_dwordx4 v[88:91], v125, s[40:41]
	s_add_i32 s13, s2, 3
	s_and_b32 s13, s13, 7
	s_lshl_b32 s14, s13, 13
	v_add_u32_e32 v125, s14, v120
	global_load_dwordx4 v[92:95], v125, s[40:41]
	s_add_i32 s13, s2, 4
	s_and_b32 s13, s13, 7
	s_lshl_b32 s14, s13, 13
	v_add_u32_e32 v125, s14, v120
	global_load_dwordx4 v[96:99], v125, s[40:41]
	s_add_i32 s13, s2, 5
	s_and_b32 s13, s13, 7
	s_lshl_b32 s14, s13, 13
	v_add_u32_e32 v125, s14, v120
	global_load_dwordx4 v[100:103], v125, s[40:41]
	s_add_i32 s13, s2, 6
	s_and_b32 s13, s13, 7
	s_lshl_b32 s14, s13, 13
	v_add_u32_e32 v125, s14, v120
	global_load_dwordx4 v[108:111], v125, s[40:41]
	s_add_i32 s13, s2, 7
	s_and_b32 s13, s13, 7
	s_lshl_b32 s14, s13, 13
	v_add_u32_e32 v125, s14, v120
	global_load_dwordx4 v[112:115], v125, s[40:41]
	global_load_dword v129, v106, s[32:33]
	global_load_dword v130, v106, s[30:31]
	s_and_b64 vcc, exec, s[6:7]
	s_cbranch_vccz .Lp_q
	v_cmp_gt_u32_e32 vcc, 32, v126
	v_mov_b32_e32 v198, 0x3db504f3
	v_mov_b32_e32 v125, s22
	v_mov_b32_e32 v104, s26
	v_cndmask_b32_e32 v198, 1.0, v198, vcc
	v_cndmask_b32_e32 v104, v104, v125, vcc
	v_mov_b32_e32 v125, s23
	v_mov_b32_e32 v105, s27
	v_cndmask_b32_e32 v105, v105, v125, vcc
	v_and_b32_e32 v196, 31, v126
	v_lshlrev_b32_e32 v196, 4, v196
	v_mov_b32_e32 v197, 0
	v_lshl_add_u64 v[104:105], v[104:105], 0, v[196:197]
	global_load_dwordx4 v[116:119], v[104:105], off
	v_lshlrev_b32_e32 v121, 14, v128
	v_lshl_add_u32 v121, v126, 4, v121
	s_and_b32 s13, s2, 15
	s_lshl_b32 s14, s13, 10
	s_add_u32 s46, s28, s14
	s_addc_u32 s47, s29, 0
	global_load_dwordx4 v[132:135], v121, s[46:47]
	s_add_i32 s13, s2, 1
	s_and_b32 s13, s13, 15
	s_lshl_b32 s14, s13, 10
	s_add_u32 s46, s28, s14
	s_addc_u32 s47, s29, 0
	global_load_dwordx4 v[136:139], v121, s[46:47]
	s_add_i32 s13, s2, 2
	s_and_b32 s13, s13, 15
	s_lshl_b32 s14, s13, 10
	s_add_u32 s46, s28, s14
	s_addc_u32 s47, s29, 0
	global_load_dwordx4 v[140:143], v121, s[46:47]
	s_add_i32 s13, s2, 3
	s_and_b32 s13, s13, 15
	s_lshl_b32 s14, s13, 10
	s_add_u32 s46, s28, s14
	s_addc_u32 s47, s29, 0
	global_load_dwordx4 v[144:147], v121, s[46:47]
	s_add_i32 s13, s2, 4
	s_and_b32 s13, s13, 15
	s_lshl_b32 s14, s13, 10
	s_add_u32 s46, s28, s14
	s_addc_u32 s47, s29, 0
	global_load_dwordx4 v[148:151], v121, s[46:47]
	s_add_i32 s13, s2, 5
	s_and_b32 s13, s13, 15
	s_lshl_b32 s14, s13, 10
	s_add_u32 s46, s28, s14
	s_addc_u32 s47, s29, 0
	global_load_dwordx4 v[152:155], v121, s[46:47]
	s_add_i32 s13, s2, 6
	s_and_b32 s13, s13, 15
	s_lshl_b32 s14, s13, 10
	s_add_u32 s46, s28, s14
	s_addc_u32 s47, s29, 0
	global_load_dwordx4 v[156:159], v121, s[46:47]
	s_add_i32 s13, s2, 7
	s_and_b32 s13, s13, 15
	s_lshl_b32 s14, s13, 10
	s_add_u32 s46, s28, s14
	s_addc_u32 s47, s29, 0
	global_load_dwordx4 v[160:163], v121, s[46:47]
	s_add_i32 s13, s2, 8
	s_and_b32 s13, s13, 15
	s_lshl_b32 s14, s13, 10
	s_add_u32 s46, s28, s14
	s_addc_u32 s47, s29, 0
	global_load_dwordx4 v[164:167], v121, s[46:47]
	s_add_i32 s13, s2, 9
	s_and_b32 s13, s13, 15
	s_lshl_b32 s14, s13, 10
	s_add_u32 s46, s28, s14
	s_addc_u32 s47, s29, 0
	global_load_dwordx4 v[168:171], v121, s[46:47]
	s_add_i32 s13, s2, 10
	s_and_b32 s13, s13, 15
	s_lshl_b32 s14, s13, 10
	s_add_u32 s46, s28, s14
	s_addc_u32 s47, s29, 0
	global_load_dwordx4 v[172:175], v121, s[46:47]
	s_add_i32 s13, s2, 11
	s_and_b32 s13, s13, 15
	s_lshl_b32 s14, s13, 10
	s_add_u32 s46, s28, s14
	s_addc_u32 s47, s29, 0
	global_load_dwordx4 v[176:179], v121, s[46:47]
	s_add_i32 s13, s2, 12
	s_and_b32 s13, s13, 15
	s_lshl_b32 s14, s13, 10
	s_add_u32 s46, s28, s14
	s_addc_u32 s47, s29, 0
	global_load_dwordx4 v[180:183], v121, s[46:47]
	s_add_i32 s13, s2, 13
	s_and_b32 s13, s13, 15
	s_lshl_b32 s14, s13, 10
	s_add_u32 s46, s28, s14
	s_addc_u32 s47, s29, 0
	global_load_dwordx4 v[184:187], v121, s[46:47]
	s_add_i32 s13, s2, 14
	s_and_b32 s13, s13, 15
	s_lshl_b32 s14, s13, 10
	s_add_u32 s46, s28, s14
	s_addc_u32 s47, s29, 0
	global_load_dwordx4 v[188:191], v121, s[46:47]
	s_add_i32 s13, s2, 15
	s_and_b32 s13, s13, 15
	s_lshl_b32 s14, s13, 10
	s_add_u32 s46, s28, s14
	s_addc_u32 s47, s29, 0
	global_load_dwordx4 v[192:195], v121, s[46:47]
	v_mul_u32_u24_e32 v59, 0x1040, v128
	v_lshl_add_u32 v59, v126, 2, v59
	v_add_u32_e32 v59, 0x11000, v59
	v_mul_u32_u24_e32 v76, 0x1100, v128
	v_lshl_add_u32 v76, v126, 3, v76
	v_add_u32_e32 v76, 0x8700, v76
	v_lshrrev_b32_e32 v77, 2, v126
	v_mul_u32_u24_e32 v77, 0x104, v77
	v_mul_u32_u24_e32 v125, 0x1040, v128
	v_add_u32_e32 v77, v77, v125
	v_and_b32_e32 v125, 3, v126
	v_lshl_add_u32 v77, v125, 6, v77
	v_add_u32_e32 v77, 0x11000, v77
	s_waitcnt vmcnt(27)
	v_cvt_pk_bf16_f32 v12, v2, v3
	v_cvt_pk_bf16_f32 v13, v4, v5
	ds_write_b64 v124, v[12:13]
	s_waitcnt vmcnt(26)
	v_cvt_pk_bf16_f32 v6, v80, v81
	v_cvt_pk_bf16_f32 v7, v82, v83
	s_and_b32 s13, s2, 7
	s_mul_i32 s14, s13, 0x1100
	v_add_u32_e32 v125, s14, v58
	ds_write_b64 v125, v[6:7]
	s_waitcnt vmcnt(25)
	v_cvt_pk_bf16_f32 v8, v84, v85
	v_cvt_pk_bf16_f32 v9, v86, v87
	s_add_i32 s13, s2, 1
	s_and_b32 s13, s13, 7
	s_mul_i32 s14, s13, 0x1100
	v_add_u32_e32 v10, s14, v58
	ds_write_b64 v10, v[8:9]
	s_waitcnt vmcnt(24)
	v_cvt_pk_bf16_f32 v6, v88, v89
	v_cvt_pk_bf16_f32 v7, v90, v91
	s_add_i32 s13, s2, 2
	s_and_b32 s13, s13, 7
	s_mul_i32 s14, s13, 0x1100
	v_add_u32_e32 v125, s14, v58
	ds_write_b64 v125, v[6:7]
	s_waitcnt vmcnt(23)
	v_cvt_pk_bf16_f32 v8, v92, v93
	v_cvt_pk_bf16_f32 v9, v94, v95
	s_add_i32 s13, s2, 3
	s_and_b32 s13, s13, 7
	s_mul_i32 s14, s13, 0x1100
	v_add_u32_e32 v10, s14, v58
	ds_write_b64 v10, v[8:9]
	s_waitcnt vmcnt(22)
	v_cvt_pk_bf16_f32 v6, v96, v97
	v_cvt_pk_bf16_f32 v7, v98, v99
	s_add_i32 s13, s2, 4
	s_and_b32 s13, s13, 7
	s_mul_i32 s14, s13, 0x1100
	v_add_u32_e32 v125, s14, v58
	ds_write_b64 v125, v[6:7]
	s_waitcnt vmcnt(21)
	v_cvt_pk_bf16_f32 v8, v100, v101
	v_cvt_pk_bf16_f32 v9, v102, v103
	s_add_i32 s13, s2, 5
	s_and_b32 s13, s13, 7
	s_mul_i32 s14, s13, 0x1100
	v_add_u32_e32 v10, s14, v58
	ds_write_b64 v10, v[8:9]
	s_waitcnt vmcnt(20)
	v_cvt_pk_bf16_f32 v6, v108, v109
	v_cvt_pk_bf16_f32 v7, v110, v111
	s_add_i32 s13, s2, 6
	s_and_b32 s13, s13, 7
	s_mul_i32 s14, s13, 0x1100
	v_add_u32_e32 v125, s14, v58
	ds_write_b64 v125, v[6:7]
	s_waitcnt vmcnt(19)
	v_cvt_pk_bf16_f32 v8, v112, v113
	v_cvt_pk_bf16_f32 v9, v114, v115
	s_add_i32 s13, s2, 7
	s_and_b32 s13, s13, 7
	s_mul_i32 s14, s13, 0x1100
	v_add_u32_e32 v10, s14, v58
	ds_write_b64 v10, v[8:9]
	s_waitcnt vmcnt(16)
	v_pk_mul_f32 v[116:117], v[198:199], v[116:117] op_sel_hi:[0,1]
	v_pk_mul_f32 v[118:119], v[198:199], v[118:119] op_sel_hi:[0,1]
	s_waitcnt vmcnt(15)
	v_mul_f32_e32 v6, v117, v133
	v_mul_f32_e32 v7, v119, v135
	v_fmac_f32_e32 v6, v116, v132
	v_fmac_f32_e32 v7, v118, v134
	s_and_b32 s13, s2, 15
	s_mul_i32 s14, s13, 0x104
	s_mul_i32 s15, s13, 0x110
	v_add_f32_e32 v6, v6, v7
	v_add_u32_e32 v125, s14, v59
	ds_write_b32 v125, v6
	v_cvt_pk_bf16_f32 v8, v132, v133
	v_cvt_pk_bf16_f32 v9, v134, v135
	v_add_u32_e32 v10, s15, v76
	s_mov_b64 exec, s[48:49]
	ds_write_b64 v10, v[8:9]
	s_mov_b64 exec, -1
	s_waitcnt vmcnt(14)
	v_mul_f32_e32 v11, v117, v137
	v_mul_f32_e32 v15, v119, v139
	v_fmac_f32_e32 v11, v116, v136
	v_fmac_f32_e32 v15, v118, v138
	s_add_i32 s13, s2, 1
	s_and_b32 s13, s13, 15
	s_mul_i32 s14, s13, 0x104
	s_mul_i32 s15, s13, 0x110
	v_add_f32_e32 v11, v11, v15
	v_add_u32_e32 v16, s14, v59
	ds_write_b32 v16, v11
	v_cvt_pk_bf16_f32 v12, v136, v137
	v_cvt_pk_bf16_f32 v13, v138, v139
	v_add_u32_e32 v14, s15, v76
	s_mov_b64 exec, s[48:49]
	ds_write_b64 v14, v[12:13]
	s_mov_b64 exec, -1
	s_waitcnt vmcnt(13)
	v_mul_f32_e32 v6, v117, v141
	v_mul_f32_e32 v7, v119, v143
	v_fmac_f32_e32 v6, v116, v140
	v_fmac_f32_e32 v7, v118, v142
	s_add_i32 s13, s2, 2
	s_and_b32 s13, s13, 15
	s_mul_i32 s14, s13, 0x104
	s_mul_i32 s15, s13, 0x110
	v_add_f32_e32 v6, v6, v7
	v_add_u32_e32 v125, s14, v59
	ds_write_b32 v125, v6
	v_cvt_pk_bf16_f32 v8, v140, v141
	v_cvt_pk_bf16_f32 v9, v142, v143
	v_add_u32_e32 v10, s15, v76
	s_mov_b64 exec, s[48:49]
	ds_write_b64 v10, v[8:9]
	s_mov_b64 exec, -1
	s_waitcnt vmcnt(12)
	v_mul_f32_e32 v11, v117, v145
	v_mul_f32_e32 v15, v119, v147
	v_fmac_f32_e32 v11, v116, v144
	v_fmac_f32_e32 v15, v118, v146
	s_add_i32 s13, s2, 3
	s_and_b32 s13, s13, 15
	s_mul_i32 s14, s13, 0x104
	s_mul_i32 s15, s13, 0x110
	v_add_f32_e32 v11, v11, v15
	v_add_u32_e32 v16, s14, v59
	ds_write_b32 v16, v11
	v_cvt_pk_bf16_f32 v12, v144, v145
	v_cvt_pk_bf16_f32 v13, v146, v147
	v_add_u32_e32 v14, s15, v76
	s_mov_b64 exec, s[48:49]
	ds_write_b64 v14, v[12:13]
	s_mov_b64 exec, -1
	s_waitcnt vmcnt(11)
	v_mul_f32_e32 v6, v117, v149
	v_mul_f32_e32 v7, v119, v151
	v_fmac_f32_e32 v6, v116, v148
	v_fmac_f32_e32 v7, v118, v150
	s_add_i32 s13, s2, 4
	s_and_b32 s13, s13, 15
	s_mul_i32 s14, s13, 0x104
	s_mul_i32 s15, s13, 0x110
	v_add_f32_e32 v6, v6, v7
	v_add_u32_e32 v125, s14, v59
	ds_write_b32 v125, v6
	v_cvt_pk_bf16_f32 v8, v148, v149
	v_cvt_pk_bf16_f32 v9, v150, v151
	v_add_u32_e32 v10, s15, v76
	s_mov_b64 exec, s[48:49]
	ds_write_b64 v10, v[8:9]
	s_mov_b64 exec, -1
	s_waitcnt vmcnt(10)
	v_mul_f32_e32 v11, v117, v153
	v_mul_f32_e32 v15, v119, v155
	v_fmac_f32_e32 v11, v116, v152
	v_fmac_f32_e32 v15, v118, v154
	s_add_i32 s13, s2, 5
	s_and_b32 s13, s13, 15
	s_mul_i32 s14, s13, 0x104
	s_mul_i32 s15, s13, 0x110
	v_add_f32_e32 v11, v11, v15
	v_add_u32_e32 v16, s14, v59
	ds_write_b32 v16, v11
	v_cvt_pk_bf16_f32 v12, v152, v153
	v_cvt_pk_bf16_f32 v13, v154, v155
	v_add_u32_e32 v14, s15, v76
	s_mov_b64 exec, s[48:49]
	ds_write_b64 v14, v[12:13]
	s_mov_b64 exec, -1
	s_waitcnt vmcnt(9)
	v_mul_f32_e32 v6, v117, v157
	v_mul_f32_e32 v7, v119, v159
	v_fmac_f32_e32 v6, v116, v156
	v_fmac_f32_e32 v7, v118, v158
	s_add_i32 s13, s2, 6
	s_and_b32 s13, s13, 15
	s_mul_i32 s14, s13, 0x104
	s_mul_i32 s15, s13, 0x110
	v_add_f32_e32 v6, v6, v7
	v_add_u32_e32 v125, s14, v59
	ds_write_b32 v125, v6
	v_cvt_pk_bf16_f32 v8, v156, v157
	v_cvt_pk_bf16_f32 v9, v158, v159
	v_add_u32_e32 v10, s15, v76
	s_mov_b64 exec, s[48:49]
	ds_write_b64 v10, v[8:9]
	s_mov_b64 exec, -1
	s_waitcnt vmcnt(8)
	v_mul_f32_e32 v11, v117, v161
	v_mul_f32_e32 v15, v119, v163
	v_fmac_f32_e32 v11, v116, v160
	v_fmac_f32_e32 v15, v118, v162
	s_add_i32 s13, s2, 7
	s_and_b32 s13, s13, 15
	s_mul_i32 s14, s13, 0x104
	s_mul_i32 s15, s13, 0x110
	v_add_f32_e32 v11, v11, v15
	v_add_u32_e32 v16, s14, v59
	ds_write_b32 v16, v11
	v_cvt_pk_bf16_f32 v12, v160, v161
	v_cvt_pk_bf16_f32 v13, v162, v163
	v_add_u32_e32 v14, s15, v76
	s_mov_b64 exec, s[48:49]
	ds_write_b64 v14, v[12:13]
	s_mov_b64 exec, -1
	s_waitcnt vmcnt(7)
	v_mul_f32_e32 v6, v117, v165
	v_mul_f32_e32 v7, v119, v167
	v_fmac_f32_e32 v6, v116, v164
	v_fmac_f32_e32 v7, v118, v166
	s_add_i32 s13, s2, 8
	s_and_b32 s13, s13, 15
	s_mul_i32 s14, s13, 0x104
	s_mul_i32 s15, s13, 0x110
	v_add_f32_e32 v6, v6, v7
	v_add_u32_e32 v125, s14, v59
	ds_write_b32 v125, v6
	v_cvt_pk_bf16_f32 v8, v164, v165
	v_cvt_pk_bf16_f32 v9, v166, v167
	v_add_u32_e32 v10, s15, v76
	s_mov_b64 exec, s[48:49]
	ds_write_b64 v10, v[8:9]
	s_mov_b64 exec, -1
	s_waitcnt vmcnt(6)
	v_mul_f32_e32 v11, v117, v169
	v_mul_f32_e32 v15, v119, v171
	v_fmac_f32_e32 v11, v116, v168
	v_fmac_f32_e32 v15, v118, v170
	s_add_i32 s13, s2, 9
	s_and_b32 s13, s13, 15
	s_mul_i32 s14, s13, 0x104
	s_mul_i32 s15, s13, 0x110
	v_add_f32_e32 v11, v11, v15
	v_add_u32_e32 v16, s14, v59
	ds_write_b32 v16, v11
	v_cvt_pk_bf16_f32 v12, v168, v169
	v_cvt_pk_bf16_f32 v13, v170, v171
	v_add_u32_e32 v14, s15, v76
	s_mov_b64 exec, s[48:49]
	ds_write_b64 v14, v[12:13]
	s_mov_b64 exec, -1
	s_waitcnt vmcnt(5)
	v_mul_f32_e32 v6, v117, v173
	v_mul_f32_e32 v7, v119, v175
	v_fmac_f32_e32 v6, v116, v172
	v_fmac_f32_e32 v7, v118, v174
	s_add_i32 s13, s2, 10
	s_and_b32 s13, s13, 15
	s_mul_i32 s14, s13, 0x104
	s_mul_i32 s15, s13, 0x110
	v_add_f32_e32 v6, v6, v7
	v_add_u32_e32 v125, s14, v59
	ds_write_b32 v125, v6
	v_cvt_pk_bf16_f32 v8, v172, v173
	v_cvt_pk_bf16_f32 v9, v174, v175
	v_add_u32_e32 v10, s15, v76
	s_mov_b64 exec, s[48:49]
	ds_write_b64 v10, v[8:9]
	s_mov_b64 exec, -1
	s_waitcnt vmcnt(4)
	v_mul_f32_e32 v11, v117, v177
	v_mul_f32_e32 v15, v119, v179
	v_fmac_f32_e32 v11, v116, v176
	v_fmac_f32_e32 v15, v118, v178
	s_add_i32 s13, s2, 11
	s_and_b32 s13, s13, 15
	s_mul_i32 s14, s13, 0x104
	s_mul_i32 s15, s13, 0x110
	v_add_f32_e32 v11, v11, v15
	v_add_u32_e32 v16, s14, v59
	ds_write_b32 v16, v11
	v_cvt_pk_bf16_f32 v12, v176, v177
	v_cvt_pk_bf16_f32 v13, v178, v179
	v_add_u32_e32 v14, s15, v76
	s_mov_b64 exec, s[48:49]
	ds_write_b64 v14, v[12:13]
	s_mov_b64 exec, -1
	s_waitcnt vmcnt(3)
	v_mul_f32_e32 v6, v117, v181
	v_mul_f32_e32 v7, v119, v183
	v_fmac_f32_e32 v6, v116, v180
	v_fmac_f32_e32 v7, v118, v182
	s_add_i32 s13, s2, 12
	s_and_b32 s13, s13, 15
	s_mul_i32 s14, s13, 0x104
	s_mul_i32 s15, s13, 0x110
	v_add_f32_e32 v6, v6, v7
	v_add_u32_e32 v125, s14, v59
	ds_write_b32 v125, v6
	v_cvt_pk_bf16_f32 v8, v180, v181
	v_cvt_pk_bf16_f32 v9, v182, v183
	v_add_u32_e32 v10, s15, v76
	s_mov_b64 exec, s[48:49]
	ds_write_b64 v10, v[8:9]
	s_mov_b64 exec, -1
	s_waitcnt vmcnt(2)
	v_mul_f32_e32 v11, v117, v185
	v_mul_f32_e32 v15, v119, v187
	v_fmac_f32_e32 v11, v116, v184
	v_fmac_f32_e32 v15, v118, v186
	s_add_i32 s13, s2, 13
	s_and_b32 s13, s13, 15
	s_mul_i32 s14, s13, 0x104
	s_mul_i32 s15, s13, 0x110
	v_add_f32_e32 v11, v11, v15
	v_add_u32_e32 v16, s14, v59
	ds_write_b32 v16, v11
	v_cvt_pk_bf16_f32 v12, v184, v185
	v_cvt_pk_bf16_f32 v13, v186, v187
	v_add_u32_e32 v14, s15, v76
	s_mov_b64 exec, s[48:49]
	ds_write_b64 v14, v[12:13]
	s_mov_b64 exec, -1
	s_waitcnt vmcnt(1)
	v_mul_f32_e32 v6, v117, v189
	v_mul_f32_e32 v7, v119, v191
	v_fmac_f32_e32 v6, v116, v188
	v_fmac_f32_e32 v7, v118, v190
	s_add_i32 s13, s2, 14
	s_and_b32 s13, s13, 15
	s_mul_i32 s14, s13, 0x104
	s_mul_i32 s15, s13, 0x110
	v_add_f32_e32 v6, v6, v7
	v_add_u32_e32 v125, s14, v59
	ds_write_b32 v125, v6
	v_cvt_pk_bf16_f32 v8, v188, v189
	v_cvt_pk_bf16_f32 v9, v190, v191
	v_add_u32_e32 v10, s15, v76
	s_mov_b64 exec, s[48:49]
	ds_write_b64 v10, v[8:9]
	s_mov_b64 exec, -1
	s_waitcnt vmcnt(0)
	v_mul_f32_e32 v11, v117, v193
	v_mul_f32_e32 v15, v119, v195
	v_fmac_f32_e32 v11, v116, v192
	v_fmac_f32_e32 v15, v118, v194
	s_add_i32 s13, s2, 15
	s_and_b32 s13, s13, 15
	s_mul_i32 s14, s13, 0x104
	s_mul_i32 s15, s13, 0x110
	v_add_f32_e32 v11, v11, v15
	v_add_u32_e32 v16, s14, v59
	ds_write_b32 v16, v11
	v_cvt_pk_bf16_f32 v12, v192, v193
	v_cvt_pk_bf16_f32 v13, v194, v195
	v_add_u32_e32 v14, s15, v76
	s_mov_b64 exec, s[48:49]
	ds_write_b64 v14, v[12:13]
	s_mov_b64 exec, -1
	s_waitcnt lgkmcnt(0)
	ds_read2_b32 v[60:61], v77 offset0:0 offset1:1
	ds_read2_b32 v[62:63], v77 offset0:2 offset1:3
	ds_read2_b32 v[64:65], v77 offset0:4 offset1:5
	ds_read2_b32 v[66:67], v77 offset0:6 offset1:7
	ds_read2_b32 v[68:69], v77 offset0:8 offset1:9
	ds_read2_b32 v[70:71], v77 offset0:10 offset1:11
	ds_read2_b32 v[72:73], v77 offset0:12 offset1:13
	ds_read2_b32 v[74:75], v77 offset0:14 offset1:15
	s_waitcnt lgkmcnt(0)
	v_add_f32_e32 v78, 0, v60
	v_add_f32_e32 v78, v78, v61
	v_add_f32_e32 v78, v78, v62
	v_add_f32_e32 v78, v78, v63
	v_add_f32_e32 v78, v78, v64
	v_add_f32_e32 v78, v78, v65
	v_add_f32_e32 v78, v78, v66
	v_add_f32_e32 v78, v78, v67
	v_add_f32_e32 v78, v78, v68
	v_add_f32_e32 v78, v78, v69
	v_add_f32_e32 v78, v78, v70
	v_add_f32_e32 v78, v78, v71
	v_add_f32_e32 v78, v78, v72
	v_add_f32_e32 v78, v78, v73
	v_add_f32_e32 v78, v78, v74
	v_add_f32_e32 v78, v78, v75
	s_nop 1
	v_add_f32_dpp v78, v78, v78 quad_perm:[1,0,3,2] row_mask:0xf bank_mask:0xf bound_ctrl:1
	s_nop 1
	v_add_f32_dpp v78, v78, v78 quad_perm:[2,3,0,1] row_mask:0xf bank_mask:0xf bound_ctrl:1
	v_lshlrev_b32_e32 v79, 4, v1
	ds_bpermute_b32 v78, v79, v78
	s_waitcnt lgkmcnt(0)
	s_barrier
	global_load_dwordx4 v[2:5], v123, s[34:35] nt
	global_load_dwordx4 v[6:9], v123, s[34:35] offset:1024 nt
	global_load_dwordx4 v[10:13], v123, s[34:35] offset:2048 nt
	global_load_dwordx4 v[14:17], v123, s[34:35] offset:3072 nt
	ds_read_b128 v[28:31], v53
	ds_read_b128 v[60:63], v56
	ds_read_b128 v[32:35], v53 offset:64
	ds_read_b128 v[64:67], v56 offset:64
	ds_read_b128 v[36:39], v53 offset:128
	ds_read_b128 v[68:71], v56 offset:128
	ds_read_b128 v[40:43], v53 offset:192
	ds_read_b128 v[72:75], v56 offset:192
	s_waitcnt lgkmcnt(6)
	v_mfma_f32_16x16x32_bf16 v[18:21], v[28:31], v[60:63], 0
	s_waitcnt lgkmcnt(4)
	v_mfma_f32_16x16x32_bf16 v[18:21], v[32:35], v[64:67], v[18:21]
	s_waitcnt lgkmcnt(2)
	v_mfma_f32_16x16x32_bf16 v[18:21], v[36:39], v[68:71], v[18:21]
	s_waitcnt lgkmcnt(0)
	v_mfma_f32_16x16x32_bf16 v[18:21], v[40:43], v[72:75], v[18:21]
	s_nop 7
	v_mul_f32_e32 v18, s44, v18
	v_mul_f32_e32 v19, s44, v19
	v_mul_f32_e32 v20, s44, v20
	v_mul_f32_e32 v21, s44, v21
	v_cvt_pk_bf16_f32 v18, v18, v18
	v_cvt_pk_bf16_f32 v19, v19, v19
	v_cvt_pk_bf16_f32 v20, v20, v20
	v_cvt_pk_bf16_f32 v21, v21, v21
	ds_write_b16 v55, v18
	ds_write_b16 v55, v19 offset:272
	ds_write_b16 v55, v20 offset:544
	ds_write_b16 v55, v21 offset:816
	s_waitcnt lgkmcnt(0)
	s_barrier
	ds_read_b128 v[28:31], v54
	ds_read_b128 v[60:63], v57
	ds_read_b128 v[32:35], v54 offset:64
	ds_read_b128 v[64:67], v57 offset:64
	ds_read_b128 v[36:39], v54 offset:128
	ds_read_b128 v[68:71], v57 offset:128
	ds_read_b128 v[40:43], v54 offset:192
	ds_read_b128 v[72:75], v57 offset:192
	s_waitcnt lgkmcnt(6)
	v_mfma_f32_16x16x32_bf16 v[18:21], v[28:31], v[60:63], 0
	s_waitcnt lgkmcnt(4)
	v_mfma_f32_16x16x32_bf16 v[18:21], v[32:35], v[64:67], v[18:21]
	s_waitcnt lgkmcnt(2)
	v_mfma_f32_16x16x32_bf16 v[18:21], v[36:39], v[68:71], v[18:21]
	s_waitcnt lgkmcnt(0)
	v_mfma_f32_16x16x32_bf16 v[18:21], v[40:43], v[72:75], v[18:21]
	s_load_dwordx2 s[4:5], s[0:1], 0x70
	s_nop 4
	v_add_f32_e32 v34, v130, v78
	v_lshl_or_b32 v30, v24, 2, s3
	v_lshlrev_b32_e32 v30, 9, v30
	v_add_u32_e32 v30, v30, v106
	v_add_u32_e32 v37, v27, v25
	v_add_u32_e32 v37, 0x19200, v37
	v_add_f32_e32 v80, v34, v18
	v_add_f32_e32 v81, v34, v19
	v_add_f32_e32 v82, v34, v20
	v_add_f32_e32 v83, v34, v21
	s_waitcnt lgkmcnt(0)
	global_store_dword v30, v80, s[4:5] sc1
	global_store_dword v30, v81, s[4:5] offset:512 sc1
	global_store_dword v30, v82, s[4:5] offset:1024 sc1
	global_store_dword v30, v83, s[4:5] offset:1536 sc1
	v_add_f32_e32 v84, v80, v80
	v_add_f32_e32 v85, v81, v81
	v_add_f32_e32 v86, v82, v82
	v_add_f32_e32 v87, v83, v83
	v_mul_f32_e32 v84, 0x3fb8aa3b, v84
	v_mul_f32_e32 v85, 0x3fb8aa3b, v85
	v_mul_f32_e32 v86, 0x3fb8aa3b, v86
	v_mul_f32_e32 v87, 0x3fb8aa3b, v87
	v_exp_f32_e32 v84, v84
	v_exp_f32_e32 v85, v85
	v_exp_f32_e32 v86, v86
	v_exp_f32_e32 v87, v87
	v_add_f32_e32 v84, 1.0, v84
	v_add_f32_e32 v85, 1.0, v85
	v_add_f32_e32 v86, 1.0, v86
	v_add_f32_e32 v87, 1.0, v87
	v_rcp_f32_e32 v84, v84
	v_rcp_f32_e32 v85, v85
	v_rcp_f32_e32 v86, v86
	v_rcp_f32_e32 v87, v87
	v_fma_f32 v84, v84, -2.0, 1.0
	v_fma_f32 v85, v85, -2.0, 1.0
	v_fma_f32 v86, v86, -2.0, 1.0
	v_fma_f32 v87, v87, -2.0, 1.0
	v_fma_f32 v88, -v84, v84, 1.0
	v_fma_f32 v89, -v85, v85, 1.0
	v_fma_f32 v90, -v86, v86, 1.0
	v_fma_f32 v91, -v87, v87, 1.0
	v_mul_f32_e32 v96, v129, v84
	v_mul_f32_e32 v97, v129, v85
	v_mul_f32_e32 v98, v129, v86
	v_mul_f32_e32 v99, v129, v87
	v_mul_f32_e32 v88, v129, v88
	v_mul_f32_e32 v89, v129, v89
	v_mul_f32_e32 v90, v129, v90
	v_mul_f32_e32 v91, v129, v91
	v_mul_f32_e64 v92, v84, -v88
	v_mul_f32_e64 v93, v85, -v89
	v_mul_f32_e64 v94, v86, -v90
	v_mul_f32_e64 v95, v87, -v91
	v_add_f32_dpp v100, v96, v96 quad_perm:[1,0,3,2] row_mask:0xf bank_mask:0xf
	v_add_f32_dpp v101, v97, v97 quad_perm:[1,0,3,2] row_mask:0xf bank_mask:0xf
	v_add_f32_dpp v102, v98, v98 quad_perm:[1,0,3,2] row_mask:0xf bank_mask:0xf
	v_add_f32_dpp v103, v99, v99 quad_perm:[1,0,3,2] row_mask:0xf bank_mask:0xf
	v_add_f32_dpp v96, v100, v100 quad_perm:[2,3,0,1] row_mask:0xf bank_mask:0xf
	v_add_f32_dpp v97, v101, v101 quad_perm:[2,3,0,1] row_mask:0xf bank_mask:0xf
	v_add_f32_dpp v98, v102, v102 quad_perm:[2,3,0,1] row_mask:0xf bank_mask:0xf
	v_add_f32_dpp v99, v103, v103 quad_perm:[2,3,0,1] row_mask:0xf bank_mask:0xf
	v_cvt_pk_bf16_f32 v88, v88, v88
	v_cvt_pk_bf16_f32 v89, v89, v89
	v_cvt_pk_bf16_f32 v90, v90, v90
	v_cvt_pk_bf16_f32 v91, v91, v91
	v_add_f32_dpp v100, v96, v96 row_half_mirror row_mask:0xf bank_mask:0xf
	v_add_f32_dpp v101, v97, v97 row_half_mirror row_mask:0xf bank_mask:0xf
	v_add_f32_dpp v102, v98, v98 row_half_mirror row_mask:0xf bank_mask:0xf
	v_add_f32_dpp v103, v99, v99 row_half_mirror row_mask:0xf bank_mask:0xf
	v_cvt_pk_bf16_f32 v92, v92, v92
	v_cvt_pk_bf16_f32 v93, v93, v93
	v_cvt_pk_bf16_f32 v94, v94, v94
	v_cvt_pk_bf16_f32 v95, v95, v95
	v_add_f32_dpp v96, v100, v100 row_mirror row_mask:0xf bank_mask:0xf
	v_add_f32_dpp v97, v101, v101 row_mirror row_mask:0xf bank_mask:0xf
	v_add_f32_dpp v98, v102, v102 row_mirror row_mask:0xf bank_mask:0xf
	v_add_f32_dpp v99, v103, v103 row_mirror row_mask:0xf bank_mask:0xf
	ds_write_b16 v37, v88
	ds_write_b16 v37, v89 offset:272
	ds_write_b16 v37, v90 offset:544
	ds_write_b16 v37, v91 offset:816
	ds_write_b16 v37, v92 offset:4352
	ds_write_b16 v37, v93 offset:4624
	ds_write_b16 v37, v94 offset:4896
	ds_write_b16 v37, v95 offset:5168
	v_mov_b32_e32 v32, 0x1d800
	v_lshl_or_b32 v32, v128, 6, v32
	v_add_u32_e32 v32, v32, v26
	v_cmp_eq_u32_e32 vcc, 0, v1
	s_and_saveexec_b64 s[8:9], vcc
	ds_write_b128 v32, v[96:99]
	s_or_b64 exec, exec, s[8:9]
	s_branch .LBB0_28
